# attention latent loop scalar clean-up: DMA blocks without s_nop pads and with incremental tile offsets, ring slot offsets rotated directly, single tile counter, K-fragment wait ladders merged pairwise
# speedup vs baseline: 1.0206x; 1.0034x over previous
.LBB0_786:
	v_and_b32_e32 v34, 63, v171
	s_lshl_b32 s16, s0, 8
	v_and_b32_e32 v35, 0x3fffffc0, v172
	v_readlane_b32 s0, v254, 42
	v_lshlrev_b32_e32 v36, 4, v34
	v_and_b32_e32 v36, 0xc0, v36
	v_lshl_add_u32 v177, v35, 2, s0
	v_lshlrev_b32_e32 v35, 3, v34
	v_lshlrev_b32_e32 v37, 1, v34
	v_and_or_b32 v36, v35, 24, v36
	v_and_b32_e32 v37, 32, v37
	v_and_b32_e32 v35, 0x100, v35
	v_or3_b32 v192, v36, v37, v35
	s_add_i32 s1, 0, 0x400
	v_add_u32_e32 v194, s1, v192
	s_add_i32 s1, 0, 0x10400
	s_waitcnt vmcnt(4)
	s_waitcnt vmcnt(7)
	ds_write_b128 v32, v[16:19] offset:17408
	s_waitcnt vmcnt(6)
	ds_write_b128 v33, v[20:23] offset:17408
	v_add_u32_e32 v16, s1, v182
	v_exp_f32_e32 v159, v0
	v_exp_f32_e32 v161, v1
	v_exp_f32_e32 v157, v2
	v_exp_f32_e32 v160, v3
	v_exp_f32_e32 v155, v4
	v_exp_f32_e32 v158, v5
	v_exp_f32_e32 v154, v6
	v_exp_f32_e32 v156, v7
	v_exp_f32_e32 v151, v8
	v_exp_f32_e32 v153, v9
	v_exp_f32_e32 v149, v10
	v_exp_f32_e32 v152, v11
	v_exp_f32_e32 v147, v12
	v_exp_f32_e32 v150, v13
	v_exp_f32_e32 v146, v14
	v_exp_f32_e32 v148, v15
	s_waitcnt vmcnt(5)
	ds_write_b128 v16, v[24:27]
	v_add_u32_e32 v16, s1, v183
	v_mov_b32_e32 v14, v113
	v_mov_b32_e32 v15, v113
	s_waitcnt vmcnt(4)
	ds_write_b128 v16, v[28:31]
	v_cmp_gt_u32_e64 s[38:39], 32, v34
	v_mov_b32_e32 v0, v113
	v_mov_b32_e32 v1, v113
	v_mov_b32_e32 v2, v113
	v_mov_b32_e32 v3, v113
	v_mov_b32_e32 v4, v113
	v_mov_b32_e32 v5, v113
	v_mov_b32_e32 v6, v113
	v_mov_b32_e32 v7, v113
	v_mov_b32_e32 v8, v113
	v_mov_b32_e32 v9, v113
	v_mov_b32_e32 v10, v113
	v_mov_b32_e32 v11, v113
	v_mov_b32_e32 v12, v113
	v_mov_b32_e32 v13, v113
	v_mov_b64_e32 v[62:63], v[14:15]
	v_mov_b64_e32 v[46:47], v[14:15]
	v_mov_b64_e32 v[30:31], v[14:15]
	s_add_i32 s16, s16, 0x8000
	s_mov_b32 s19, 2
	s_mov_b32 s28, 4
	s_mov_b32 s0, 1
	v_lshl_add_u32 v178, v173, 2, v177
	s_mov_b32 s29, 0
	v_mov_b32_e32 v179, 0
	v_mov_b64_e32 v[60:61], v[12:13]
	v_mov_b64_e32 v[58:59], v[10:11]
	v_mov_b64_e32 v[56:57], v[8:9]
	v_mov_b64_e32 v[54:55], v[6:7]
	v_mov_b64_e32 v[52:53], v[4:5]
	v_mov_b64_e32 v[50:51], v[2:3]
	v_mov_b64_e32 v[48:49], v[0:1]
	v_mov_b64_e32 v[44:45], v[12:13]
	v_mov_b64_e32 v[42:43], v[10:11]
	v_mov_b64_e32 v[40:41], v[8:9]
	v_mov_b64_e32 v[38:39], v[6:7]
	v_mov_b64_e32 v[36:37], v[4:5]
	v_mov_b64_e32 v[34:35], v[2:3]
	v_mov_b64_e32 v[32:33], v[0:1]
	v_mov_b64_e32 v[28:29], v[12:13]
	v_mov_b64_e32 v[26:27], v[10:11]
	v_mov_b64_e32 v[24:25], v[8:9]
	v_mov_b64_e32 v[22:23], v[6:7]
	v_mov_b64_e32 v[20:21], v[4:5]
	v_mov_b64_e32 v[18:19], v[2:3]
	v_mov_b64_e32 v[16:17], v[0:1]
	s_waitcnt lgkmcnt(0)
	s_add_u32 s78, s8, s96
	s_addc_u32 s79, s9, 0
	s_add_u32 s80, s6, s96
	s_addc_u32 s81, s7, 0
	v_and_b32_e32 v183, 7, v181
	v_lshrrev_b32_e32 v185, 4, v181
	v_lshlrev_b32_e32 v185, 3, v185
	v_xor_b32_e32 v183, v183, v185
	v_and_b32_e32 v185, 15, v172
	v_xor_b32_e32 v183, v183, v185
	v_lshlrev_b32_e32 v183, 4, v183
	v_mad_u32_u24 v183, v181, s62, v183
	v_lshrrev_b32_e32 v185, 7, v172
	v_lshlrev_b32_e32 v185, 3, v185
	v_bfe_u32 v184, v172, 2, 3
	v_add_u32_e32 v185, v185, v184
	v_bfe_u32 v184, v172, 5, 2
	v_lshlrev_b32_e32 v184, 2, v184
	v_and_b32_e32 v182, 3, v172
	v_add_u32_e32 v184, v184, v182
	v_lshlrev_b32_e32 v184, 4, v184
	v_mad_u32_u24 v185, v185, s62, v184
	v_add_u32_e32 v182, 0x30000, v183
	v_add_u32_e32 v184, 0x30000, v185
	s_mul_i32 s89, s16, 0x1800
	s_mov_b32 s21, 0x4000
	s_mov_b32 s22, 0x8000
	s_mov_b32 s20, 0
	s_mov_b32 s55, 1
	s_lshl_b32 s84, s90, 10
	s_add_i32 s65, s18, 0x80
	s_mul_i32 s65, s65, 0x1800
	s_add_u32 s66, s80, s65
	s_addc_u32 s67, s81, 0
	s_add_i32 s85, s84, 0x14400
	s_mov_b32 m0, s85
	s_nop 0
	global_load_lds_dwordx4 v183, s[66:67]
	s_add_i32 m0, s85, 0x2000
	s_nop 0
	global_load_lds_dwordx4 v182, s[66:67]
	s_barrier
.LBB0_787:
	v_add_u32_e32 v180, s21, v191
	v_add_u32_e32 v84, v180, v190
	ds_read_b128 v[80:83], v84 offset:50176
	ds_read_b128 v[84:87], v84 offset:58368
	v_add_u32_e32 v195, v180, v188
	ds_read_b128 v[196:199], v195 offset:50176
	ds_read_b128 v[200:203], v195 offset:58368
	v_add_u32_e32 v195, v180, v187
	s_waitcnt lgkmcnt(2)
	v_mfma_f32_32x32x16_bf16 v[96:111], v[80:83], v[122:125], 0
	v_add_u32_e32 v180, v180, v186
	v_exp_f32_e32 v204, v72
	v_exp_f32_e32 v205, v73
	v_exp_f32_e32 v206, v74
	v_exp_f32_e32 v207, v75
	v_exp_f32_e32 v208, v76
	v_exp_f32_e32 v209, v77
	v_mfma_f32_32x32x16_bf16 v[80:95], v[84:87], v[122:125], 0
	v_exp_f32_e32 v210, v78
	v_exp_f32_e32 v79, v79
	s_waitcnt lgkmcnt(0)
	v_mfma_f32_32x32x16_bf16 v[96:111], v[196:199], v[126:129], v[96:111]
	v_mfma_f32_32x32x16_bf16 v[80:95], v[200:203], v[126:129], v[80:95]
	ds_read_b128 v[196:199], v195 offset:50176
	ds_read_b128 v[200:203], v195 offset:58368
	s_waitcnt lgkmcnt(0)
	v_mfma_f32_32x32x16_bf16 v[96:111], v[196:199], v[118:121], v[96:111]
	v_mfma_f32_32x32x16_bf16 v[80:95], v[200:203], v[118:121], v[80:95]
	ds_read_b128 v[196:199], v180 offset:50176
	ds_read_b128 v[200:203], v180 offset:58368
	v_exp_f32_e32 v180, v64
	v_add_f32_e32 v64, v161, v159
	v_add_f32_e32 v195, v157, v160
	v_add_f32_e32 v64, v155, v64
	v_add_f32_e32 v195, v158, v195
	v_add_f32_e32 v64, v154, v64
	v_add_f32_e32 v195, v156, v195
	v_add_f32_e32 v64, v151, v64
	v_add_f32_e32 v195, v153, v195
	v_add_f32_e32 v64, v149, v64
	v_add_f32_e32 v195, v152, v195
	v_add_f32_e32 v64, v147, v64
	s_waitcnt lgkmcnt(0)
	v_mfma_f32_32x32x16_bf16 v[96:111], v[196:199], v[114:117], v[96:111]
	v_exp_f32_e32 v197, v65
	v_add_f32_e32 v195, v150, v195
	v_exp_f32_e32 v198, v66
	v_add_f32_e32 v64, v146, v64
	v_exp_f32_e32 v199, v67
	v_add_f32_e32 v195, v148, v195
	v_add_f32_e32 v64, v180, v64
	v_mfma_f32_32x32x16_bf16 v[80:95], v[200:203], v[114:117], v[80:95]
	v_exp_f32_e32 v200, v68
	v_exp_f32_e32 v201, v69
	v_add_f32_e32 v195, v197, v195
	v_exp_f32_e32 v202, v70
	v_add_f32_e32 v64, v198, v64
	v_exp_f32_e32 v203, v71
	v_add_f32_e32 v195, v199, v195
	v_add_f32_e32 v64, v200, v64
	v_add_f32_e32 v195, v201, v195
	v_add_f32_e32 v64, v202, v64
	v_add_f32_e32 v195, v203, v195
	v_add_f32_e32 v64, v204, v64
	v_add_f32_e32 v195, v205, v195
	v_add_f32_e32 v64, v206, v64
	v_add_f32_e32 v195, v207, v195
	v_add_f32_e32 v64, v208, v64
	v_add_f32_e32 v195, v209, v195
	v_add_f32_e32 v64, v210, v64
	v_add_f32_e32 v195, v79, v195
	v_add_f32_e32 v195, v195, v64
	v_cvt_pk_bf16_f32 v64, v159, v161
	v_cvt_pk_bf16_f32 v65, v157, v160
	v_cvt_pk_bf16_f32 v66, v155, v158
	v_cvt_pk_bf16_f32 v67, v154, v156
	v_cvt_pk_bf16_f32 v68, v151, v153
	v_cvt_pk_bf16_f32 v69, v149, v152
	v_cvt_pk_bf16_f32 v70, v147, v150
	v_cvt_pk_bf16_f32 v71, v146, v148
	v_cvt_pk_bf16_f32 v72, v180, v197
	v_cvt_pk_bf16_f32 v73, v198, v199
	v_cvt_pk_bf16_f32 v74, v200, v201
	v_cvt_pk_bf16_f32 v75, v202, v203
	v_cvt_pk_bf16_f32 v76, v204, v205
	v_cvt_pk_bf16_f32 v77, v206, v207
	v_cvt_pk_bf16_f32 v78, v208, v209
	v_cvt_pk_bf16_f32 v79, v210, v79
	s_add_u32 s66, s78, s65
	s_addc_u32 s67, s79, 0
	s_add_i32 s85, s22, s84
	s_add_i32 m0, s85, 0x400
	s_add_i32 s86, s20, s84
	global_load_lds_dwordx4 v185, s[66:67]
	s_add_i32 m0, s85, 0x2400
	s_add_i32 s64, s65, 0x60000
	global_load_lds_dwordx4 v184, s[66:67]
	s_add_i32 m0, s86, 0xc400
	s_add_u32 s70, s80, s64
	s_addc_u32 s71, s81, 0
	global_load_lds_dwordx4 v183, s[70:71]
	s_add_i32 m0, s86, 0xe400
	s_mov_b32 s65, s64
	global_load_lds_dwordx4 v182, s[70:71]
	v_add_u32_e32 v180, s20, v194
	ds_read_b64_tr_b16 v[198:199], v180 offset:0
	ds_read_b64_tr_b16 v[200:201], v180 offset:0x800
	ds_read_b64_tr_b16 v[202:203], v180 offset:0x1000
	ds_read_b64_tr_b16 v[204:205], v180 offset:0x1800
	ds_read_b64_tr_b16 v[206:207], v180 offset:0x2000
	ds_read_b64_tr_b16 v[208:209], v180 offset:0x2800
	ds_read_b64_tr_b16 v[222:223], v180 offset:0x3000
	ds_read_b64_tr_b16 v[224:225], v180 offset:0x3800
	s_waitcnt lgkmcnt(0)
	v_mfma_f32_32x32x16_bf16 v[0:15], v[64:67], v[198:201], v[0:15]
	ds_read_b64_tr_b16 v[198:199], v180 offset:0x200
	ds_read_b64_tr_b16 v[200:201], v180 offset:0xa00
	v_mfma_f32_32x32x16_bf16 v[0:15], v[68:71], v[202:205], v[0:15]
	ds_read_b64_tr_b16 v[202:203], v180 offset:0x1200
	ds_read_b64_tr_b16 v[204:205], v180 offset:0x1a00
	v_mfma_f32_32x32x16_bf16 v[0:15], v[72:75], v[206:209], v[0:15]
	ds_read_b64_tr_b16 v[206:207], v180 offset:0x2200
	ds_read_b64_tr_b16 v[208:209], v180 offset:0x2a00
	v_mfma_f32_32x32x16_bf16 v[0:15], v[76:79], v[222:225], v[0:15]
	ds_read_b64_tr_b16 v[222:223], v180 offset:0x3200
	ds_read_b64_tr_b16 v[224:225], v180 offset:0x3a00
	s_waitcnt lgkmcnt(0)
	v_mfma_f32_32x32x16_bf16 v[48:63], v[64:67], v[198:201], v[48:63]
	ds_read_b64_tr_b16 v[198:199], v180 offset:0x400
	ds_read_b64_tr_b16 v[200:201], v180 offset:0xc00
	v_mfma_f32_32x32x16_bf16 v[48:63], v[68:71], v[202:205], v[48:63]
	ds_read_b64_tr_b16 v[202:203], v180 offset:0x1400
	ds_read_b64_tr_b16 v[204:205], v180 offset:0x1c00
	v_mfma_f32_32x32x16_bf16 v[48:63], v[72:75], v[206:209], v[48:63]
	ds_read_b64_tr_b16 v[206:207], v180 offset:0x2400
	ds_read_b64_tr_b16 v[208:209], v180 offset:0x2c00
	v_mfma_f32_32x32x16_bf16 v[48:63], v[76:79], v[222:225], v[48:63]
	ds_read_b64_tr_b16 v[222:223], v180 offset:0x3400
	ds_read_b64_tr_b16 v[224:225], v180 offset:0x3c00
	s_waitcnt lgkmcnt(0)
	v_mfma_f32_32x32x16_bf16 v[32:47], v[64:67], v[198:201], v[32:47]
	ds_read_b64_tr_b16 v[198:199], v180 offset:0x600
	ds_read_b64_tr_b16 v[200:201], v180 offset:0xe00
	v_mfma_f32_32x32x16_bf16 v[32:47], v[68:71], v[202:205], v[32:47]
	ds_read_b64_tr_b16 v[202:203], v180 offset:0x1600
	ds_read_b64_tr_b16 v[204:205], v180 offset:0x1e00
	v_mfma_f32_32x32x16_bf16 v[32:47], v[72:75], v[206:209], v[32:47]
	ds_read_b64_tr_b16 v[206:207], v180 offset:0x2600
	ds_read_b64_tr_b16 v[208:209], v180 offset:0x2e00
	v_mfma_f32_32x32x16_bf16 v[32:47], v[76:79], v[222:225], v[32:47]
	ds_read_b64_tr_b16 v[222:223], v180 offset:0x3600
	ds_read_b64_tr_b16 v[224:225], v180 offset:0x3e00
	s_waitcnt lgkmcnt(0)
	v_mfma_f32_32x32x16_bf16 v[16:31], v[64:67], v[198:201], v[16:31]
	v_max_f32_e32 v64, v96, v97
	v_max3_f32 v65, v80, v81, v82
	v_max3_f32 v64, v64, v98, v99
	v_max3_f32 v65, v65, v83, v84
	v_max3_f32 v64, v64, v100, v101
	v_mfma_f32_32x32x16_bf16 v[16:31], v[68:71], v[202:205], v[16:31]
	v_max3_f32 v65, v65, v85, v86
	v_max3_f32 v64, v64, v102, v103
	v_max3_f32 v65, v65, v87, v88
	v_max3_f32 v64, v64, v104, v105
	v_max3_f32 v65, v65, v89, v90
	v_max3_f32 v64, v64, v106, v107
	v_max3_f32 v65, v65, v91, v92
	v_mfma_f32_32x32x16_bf16 v[16:31], v[72:75], v[206:209], v[16:31]
	v_max3_f32 v64, v64, v108, v109
	v_max3_f32 v65, v65, v93, v94
	v_max3_f32 v64, v64, v110, v111
	v_max3_f32 v64, v64, v65, v95
	v_mov_b32_e32 v198, 1.0
	v_mfma_f32_32x32x16_bf16 v[16:31], v[76:79], v[222:225], v[16:31]
	v_cmp_ge_f32_e64 s[40:41], s75, v64
	s_and_b64 s[0:1], s[56:57], s[40:41]
	s_cmp_eq_u64 s[0:1], exec
	s_cbranch_scc1 .LBB0_792
	s_branch .LBB0_801
.LBB0_788:
	v_cmp_gt_f32_e32 vcc, 1.0, v198
	s_cbranch_vccz .LBB0_792
	s_and_saveexec_b64 s[0:1], s[38:39]
	ds_write_b32 v178, v198 offset:128
	s_or_b64 exec, exec, s[0:1]
	s_waitcnt lgkmcnt(0)
	v_add_u32_e32 v76, v177, v112
	ds_read_b128 v[64:67], v76 offset:224
	ds_read_b128 v[68:71], v76 offset:192
	ds_read_b128 v[72:75], v76 offset:160
	ds_read_b128 v[76:79], v76 offset:128
	s_waitcnt lgkmcnt(3)
	v_pk_mul_f32 v[12:13], v[12:13], v[64:65]
	s_waitcnt lgkmcnt(2)
	v_pk_mul_f32 v[8:9], v[8:9], v[68:69]
	s_waitcnt lgkmcnt(1)
	v_pk_mul_f32 v[4:5], v[4:5], v[72:73]
	v_pk_mul_f32 v[14:15], v[14:15], v[66:67]
	v_pk_mul_f32 v[10:11], v[10:11], v[70:71]
	v_pk_mul_f32 v[6:7], v[6:7], v[74:75]
	s_waitcnt lgkmcnt(0)
	v_pk_mul_f32 v[2:3], v[2:3], v[78:79]
	v_pk_mul_f32 v[0:1], v[0:1], v[76:77]
	v_pk_mul_f32 v[60:61], v[60:61], v[64:65]
	v_pk_mul_f32 v[56:57], v[56:57], v[68:69]
	v_pk_mul_f32 v[52:53], v[52:53], v[72:73]
	v_pk_mul_f32 v[62:63], v[62:63], v[66:67]
	v_pk_mul_f32 v[58:59], v[58:59], v[70:71]
	v_pk_mul_f32 v[54:55], v[54:55], v[74:75]
	v_pk_mul_f32 v[50:51], v[50:51], v[78:79]
	v_pk_mul_f32 v[48:49], v[48:49], v[76:77]
	v_pk_mul_f32 v[44:45], v[44:45], v[64:65]
	v_pk_mul_f32 v[40:41], v[40:41], v[68:69]
	v_pk_mul_f32 v[36:37], v[36:37], v[72:73]
	v_pk_mul_f32 v[46:47], v[46:47], v[66:67]
	v_pk_mul_f32 v[42:43], v[42:43], v[70:71]
	v_pk_mul_f32 v[38:39], v[38:39], v[74:75]
	v_pk_mul_f32 v[34:35], v[34:35], v[78:79]
	v_pk_mul_f32 v[32:33], v[32:33], v[76:77]
	v_pk_mul_f32 v[28:29], v[28:29], v[64:65]
	v_pk_mul_f32 v[24:25], v[24:25], v[68:69]
	v_pk_mul_f32 v[20:21], v[20:21], v[72:73]
	v_pk_mul_f32 v[30:31], v[30:31], v[66:67]
	v_pk_mul_f32 v[26:27], v[26:27], v[70:71]
	v_pk_mul_f32 v[22:23], v[22:23], v[74:75]
	v_pk_mul_f32 v[18:19], v[18:19], v[78:79]
	v_pk_mul_f32 v[16:17], v[16:17], v[76:77]
.LBB0_792:
	v_exp_f32_e32 v197, v96
	v_exp_f32_e32 v208, v97
	v_exp_f32_e32 v209, v98
	v_exp_f32_e32 v210, v99
	v_exp_f32_e32 v211, v100
	v_exp_f32_e32 v220, v101
	v_exp_f32_e32 v221, v102
	v_exp_f32_e32 v222, v103
	v_exp_f32_e32 v223, v104
	v_exp_f32_e32 v224, v105
	v_exp_f32_e32 v225, v106
	v_exp_f32_e32 v226, v107
	v_exp_f32_e32 v227, v108
	v_exp_f32_e32 v228, v109
	v_exp_f32_e32 v229, v110
	v_exp_f32_e32 v230, v111
	s_waitcnt vmcnt(4) lgkmcnt(0)
	s_barrier
	v_add_u32_e32 v199, s22, v189
	v_add_u32_e32 v68, v199, v190
	ds_read_b128 v[64:67], v68 offset:50176
	ds_read_b128 v[68:71], v68 offset:58368
	v_add_u32_e32 v204, v199, v188
	ds_read_b128 v[200:203], v204 offset:50176
	ds_read_b128 v[204:207], v204 offset:58368
	v_exp_f32_e32 v231, v87
	s_waitcnt lgkmcnt(2)
	v_mfma_f32_32x32x16_bf16 v[96:111], v[64:67], v[122:125], 0
	v_exp_f32_e32 v232, v88
	v_exp_f32_e32 v233, v89
	v_exp_f32_e32 v234, v90
	v_exp_f32_e32 v235, v91
	v_exp_f32_e32 v236, v92
	v_exp_f32_e32 v237, v93
	v_exp_f32_e32 v238, v94
	v_mfma_f32_32x32x16_bf16 v[64:79], v[68:71], v[122:125], 0
	v_exp_f32_e32 v95, v95
	s_waitcnt lgkmcnt(0)
	v_mfma_f32_32x32x16_bf16 v[96:111], v[200:203], v[126:129], v[96:111]
	v_mfma_f32_32x32x16_bf16 v[64:79], v[204:207], v[126:129], v[64:79]
	v_add_u32_e32 v204, v199, v187
	ds_read_b128 v[200:203], v204 offset:50176
	ds_read_b128 v[204:207], v204 offset:58368
	v_add_u32_e32 v199, v199, v186
	s_waitcnt lgkmcnt(0)
	v_mfma_f32_32x32x16_bf16 v[96:111], v[200:203], v[118:121], v[96:111]
	v_mfma_f32_32x32x16_bf16 v[64:79], v[204:207], v[118:121], v[64:79]
	ds_read_b128 v[200:203], v199 offset:50176
	ds_read_b128 v[204:207], v199 offset:58368
	s_waitcnt lgkmcnt(0)
	v_mfma_f32_32x32x16_bf16 v[96:111], v[200:203], v[114:117], v[96:111]
	v_exp_f32_e32 v201, v80
	v_add_f32_e32 v80, v208, v197
	v_add_f32_e32 v199, v209, v210
	v_add_f32_e32 v80, v211, v80
	v_add_f32_e32 v199, v220, v199
	v_add_f32_e32 v80, v221, v80
	v_add_f32_e32 v199, v222, v199
	v_add_f32_e32 v80, v223, v80
	v_add_f32_e32 v199, v224, v199
	v_add_f32_e32 v80, v225, v80
	v_add_f32_e32 v199, v226, v199
	v_add_f32_e32 v80, v227, v80
	v_exp_f32_e32 v202, v81
	v_add_f32_e32 v199, v228, v199
	v_exp_f32_e32 v203, v82
	v_add_f32_e32 v80, v229, v80
	v_mfma_f32_32x32x16_bf16 v[64:79], v[204:207], v[114:117], v[64:79]
	v_exp_f32_e32 v204, v83
	v_add_f32_e32 v199, v230, v199
	v_exp_f32_e32 v205, v84
	v_add_f32_e32 v80, v201, v80
	v_exp_f32_e32 v206, v85
	v_add_f32_e32 v199, v202, v199
	v_exp_f32_e32 v207, v86
	v_add_f32_e32 v80, v203, v80
	v_add_f32_e32 v199, v204, v199
	v_add_f32_e32 v80, v205, v80
	v_add_f32_e32 v199, v206, v199
	v_add_f32_e32 v80, v207, v80
	v_add_f32_e32 v199, v231, v199
	v_add_f32_e32 v80, v232, v80
	v_add_f32_e32 v199, v233, v199
	v_add_f32_e32 v80, v234, v80
	v_add_f32_e32 v199, v235, v199
	v_add_f32_e32 v80, v236, v80
	v_add_f32_e32 v199, v237, v199
	v_add_f32_e32 v80, v238, v80
	v_add_f32_e32 v199, v95, v199
	v_add_f32_e32 v199, v199, v80
	v_cvt_pk_bf16_f32 v80, v197, v208
	v_cvt_pk_bf16_f32 v81, v209, v210
	v_cvt_pk_bf16_f32 v82, v211, v220
	v_cvt_pk_bf16_f32 v83, v221, v222
	v_cvt_pk_bf16_f32 v84, v223, v224
	v_cvt_pk_bf16_f32 v85, v225, v226
	v_cvt_pk_bf16_f32 v86, v227, v228
	v_cvt_pk_bf16_f32 v87, v229, v230
	v_cvt_pk_bf16_f32 v88, v201, v202
	v_cvt_pk_bf16_f32 v89, v203, v204
	v_cvt_pk_bf16_f32 v90, v205, v206
	v_cvt_pk_bf16_f32 v91, v207, v231
	v_cvt_pk_bf16_f32 v92, v232, v233
	v_cvt_pk_bf16_f32 v93, v234, v235
	v_cvt_pk_bf16_f32 v94, v236, v237
	v_cvt_pk_bf16_f32 v95, v238, v95
	s_add_u32 s66, s78, s65
	s_addc_u32 s67, s79, 0
	s_add_i32 s85, s20, s84
	s_add_i32 m0, s85, 0x400
	s_add_i32 s86, s21, s84
	global_load_lds_dwordx4 v185, s[66:67]
	s_add_i32 m0, s85, 0x2400
	s_add_i32 s64, s65, 0x60000
	global_load_lds_dwordx4 v184, s[66:67]
	s_cmp_eq_u32 s55, 29
	s_cselect_b32 s64, s89, s64
	s_add_i32 m0, s86, 0xc400
	s_add_u32 s70, s80, s64
	s_addc_u32 s71, s81, 0
	global_load_lds_dwordx4 v183, s[70:71]
	s_add_i32 m0, s86, 0xe400
	s_mov_b32 s65, s64
	global_load_lds_dwordx4 v182, s[70:71]
.LBB0_794:
	v_add_u32_e32 v197, s21, v194
	ds_read_b64_tr_b16 v[202:203], v197 offset:0
	ds_read_b64_tr_b16 v[204:205], v197 offset:0x800
	ds_read_b64_tr_b16 v[206:207], v197 offset:0x1000
	ds_read_b64_tr_b16 v[208:209], v197 offset:0x1800
	ds_read_b64_tr_b16 v[222:223], v197 offset:0x2000
	ds_read_b64_tr_b16 v[224:225], v197 offset:0x2800
	ds_read_b64_tr_b16 v[226:227], v197 offset:0x3000
	ds_read_b64_tr_b16 v[228:229], v197 offset:0x3800
	s_waitcnt lgkmcnt(0)
	v_mfma_f32_32x32x16_bf16 v[0:15], v[80:83], v[202:205], v[0:15]
	ds_read_b64_tr_b16 v[202:203], v197 offset:0x200
	ds_read_b64_tr_b16 v[204:205], v197 offset:0xa00
	v_mfma_f32_32x32x16_bf16 v[0:15], v[84:87], v[206:209], v[0:15]
	ds_read_b64_tr_b16 v[206:207], v197 offset:0x1200
	ds_read_b64_tr_b16 v[208:209], v197 offset:0x1a00
	v_mfma_f32_32x32x16_bf16 v[0:15], v[88:91], v[222:225], v[0:15]
	ds_read_b64_tr_b16 v[222:223], v197 offset:0x2200
	ds_read_b64_tr_b16 v[224:225], v197 offset:0x2a00
	v_mfma_f32_32x32x16_bf16 v[0:15], v[92:95], v[226:229], v[0:15]
	ds_read_b64_tr_b16 v[226:227], v197 offset:0x3200
	ds_read_b64_tr_b16 v[228:229], v197 offset:0x3a00
	s_waitcnt lgkmcnt(0)
	v_mfma_f32_32x32x16_bf16 v[48:63], v[80:83], v[202:205], v[48:63]
	ds_read_b64_tr_b16 v[202:203], v197 offset:0x400
	ds_read_b64_tr_b16 v[204:205], v197 offset:0xc00
	v_mfma_f32_32x32x16_bf16 v[48:63], v[84:87], v[206:209], v[48:63]
	ds_read_b64_tr_b16 v[206:207], v197 offset:0x1400
	ds_read_b64_tr_b16 v[208:209], v197 offset:0x1c00
	v_mfma_f32_32x32x16_bf16 v[48:63], v[88:91], v[222:225], v[48:63]
	ds_read_b64_tr_b16 v[222:223], v197 offset:0x2400
	ds_read_b64_tr_b16 v[224:225], v197 offset:0x2c00
	v_mfma_f32_32x32x16_bf16 v[48:63], v[92:95], v[226:229], v[48:63]
	ds_read_b64_tr_b16 v[226:227], v197 offset:0x3400
	ds_read_b64_tr_b16 v[228:229], v197 offset:0x3c00
	s_waitcnt lgkmcnt(0)
	v_mfma_f32_32x32x16_bf16 v[32:47], v[80:83], v[202:205], v[32:47]
	ds_read_b64_tr_b16 v[202:203], v197 offset:0x600
	ds_read_b64_tr_b16 v[204:205], v197 offset:0xe00
	v_mfma_f32_32x32x16_bf16 v[32:47], v[84:87], v[206:209], v[32:47]
	ds_read_b64_tr_b16 v[206:207], v197 offset:0x1600
	ds_read_b64_tr_b16 v[208:209], v197 offset:0x1e00
	v_mfma_f32_32x32x16_bf16 v[32:47], v[88:91], v[222:225], v[32:47]
	ds_read_b64_tr_b16 v[222:223], v197 offset:0x2600
	ds_read_b64_tr_b16 v[224:225], v197 offset:0x2e00
	v_mfma_f32_32x32x16_bf16 v[32:47], v[92:95], v[226:229], v[32:47]
	ds_read_b64_tr_b16 v[226:227], v197 offset:0x3600
	ds_read_b64_tr_b16 v[228:229], v197 offset:0x3e00
	s_waitcnt lgkmcnt(0)
	v_mfma_f32_32x32x16_bf16 v[16:31], v[80:83], v[202:205], v[16:31]
	v_max_f32_e32 v80, v96, v97
	v_max3_f32 v81, v64, v65, v66
	v_max3_f32 v80, v80, v98, v99
	v_max3_f32 v81, v81, v67, v68
	v_max3_f32 v80, v80, v100, v101
	v_mfma_f32_32x32x16_bf16 v[16:31], v[84:87], v[206:209], v[16:31]
	v_max3_f32 v81, v81, v69, v70
	v_max3_f32 v80, v80, v102, v103
	v_max3_f32 v81, v81, v71, v72
	v_max3_f32 v80, v80, v104, v105
	v_max3_f32 v81, v81, v73, v74
	v_max3_f32 v80, v80, v106, v107
	v_max3_f32 v81, v81, v75, v76
	v_mfma_f32_32x32x16_bf16 v[16:31], v[88:91], v[222:225], v[16:31]
	v_max3_f32 v80, v80, v108, v109
	v_max3_f32 v81, v81, v77, v78
	v_max3_f32 v80, v80, v110, v111
	v_max3_f32 v80, v80, v81, v79
	v_mov_b32_e32 v197, 1.0
	v_mfma_f32_32x32x16_bf16 v[16:31], v[92:95], v[226:229], v[16:31]
	v_cmp_ge_f32_e64 s[40:41], s75, v80
	s_and_b64 s[0:1], s[56:57], s[40:41]
	s_cmp_eq_u64 s[0:1], exec
	s_cbranch_scc1 .LBB0_799
	s_branch .LBB0_802
.LBB0_795:
	v_cmp_gt_f32_e32 vcc, 1.0, v197
	s_cbranch_vccz .LBB0_799
	s_and_saveexec_b64 s[0:1], s[38:39]
	ds_write_b32 v178, v197 offset:128
	s_or_b64 exec, exec, s[0:1]
	s_waitcnt lgkmcnt(0)
	v_add_u32_e32 v92, v177, v112
	ds_read_b128 v[80:83], v92 offset:224
	ds_read_b128 v[84:87], v92 offset:192
	ds_read_b128 v[88:91], v92 offset:160
	ds_read_b128 v[92:95], v92 offset:128
	s_waitcnt lgkmcnt(3)
	v_pk_mul_f32 v[12:13], v[12:13], v[80:81]
	s_waitcnt lgkmcnt(2)
	v_pk_mul_f32 v[8:9], v[8:9], v[84:85]
	s_waitcnt lgkmcnt(1)
	v_pk_mul_f32 v[4:5], v[4:5], v[88:89]
	v_pk_mul_f32 v[14:15], v[14:15], v[82:83]
	v_pk_mul_f32 v[10:11], v[10:11], v[86:87]
	v_pk_mul_f32 v[6:7], v[6:7], v[90:91]
	s_waitcnt lgkmcnt(0)
	v_pk_mul_f32 v[2:3], v[2:3], v[94:95]
	v_pk_mul_f32 v[0:1], v[0:1], v[92:93]
	v_pk_mul_f32 v[60:61], v[60:61], v[80:81]
	v_pk_mul_f32 v[56:57], v[56:57], v[84:85]
	v_pk_mul_f32 v[52:53], v[52:53], v[88:89]
	v_pk_mul_f32 v[62:63], v[62:63], v[82:83]
	v_pk_mul_f32 v[58:59], v[58:59], v[86:87]
	v_pk_mul_f32 v[54:55], v[54:55], v[90:91]
	v_pk_mul_f32 v[50:51], v[50:51], v[94:95]
	v_pk_mul_f32 v[48:49], v[48:49], v[92:93]
	v_pk_mul_f32 v[44:45], v[44:45], v[80:81]
	v_pk_mul_f32 v[40:41], v[40:41], v[84:85]
	v_pk_mul_f32 v[36:37], v[36:37], v[88:89]
	v_pk_mul_f32 v[46:47], v[46:47], v[82:83]
	v_pk_mul_f32 v[42:43], v[42:43], v[86:87]
	v_pk_mul_f32 v[38:39], v[38:39], v[90:91]
	v_pk_mul_f32 v[34:35], v[34:35], v[94:95]
	v_pk_mul_f32 v[32:33], v[32:33], v[92:93]
	v_pk_mul_f32 v[28:29], v[28:29], v[80:81]
	v_pk_mul_f32 v[24:25], v[24:25], v[84:85]
	v_pk_mul_f32 v[20:21], v[20:21], v[88:89]
	v_pk_mul_f32 v[30:31], v[30:31], v[82:83]
	v_pk_mul_f32 v[26:27], v[26:27], v[86:87]
	v_pk_mul_f32 v[22:23], v[22:23], v[90:91]
	v_pk_mul_f32 v[18:19], v[18:19], v[94:95]
	v_pk_mul_f32 v[16:17], v[16:17], v[92:93]
.LBB0_799:
	v_exp_f32_e32 v159, v96
	v_exp_f32_e32 v161, v97
	v_exp_f32_e32 v157, v98
	v_exp_f32_e32 v160, v99
	v_exp_f32_e32 v155, v100
	v_exp_f32_e32 v158, v101
	v_exp_f32_e32 v154, v102
	v_exp_f32_e32 v156, v103
	v_exp_f32_e32 v151, v104
	v_exp_f32_e32 v153, v105
	v_exp_f32_e32 v149, v106
	v_exp_f32_e32 v152, v107
	v_exp_f32_e32 v147, v108
	v_exp_f32_e32 v150, v109
	v_exp_f32_e32 v146, v110
	v_exp_f32_e32 v148, v111
	v_fma_f32 v80, v193, v179, v195
	v_fma_f32 v179, v80, v198, v199
	s_cmp_gt_u32 s55, 32
	s_waitcnt vmcnt(4) lgkmcnt(0)
	s_barrier
	s_cbranch_scc1 .LBB0_803
	s_add_i32 s55, s55, 2
	s_mov_b32 s0, s21
	s_mov_b32 s21, s20
	s_mov_b32 s20, s22
	s_mov_b32 s22, s0
	v_mov_b32_e32 v193, v197
	s_branch .LBB0_787
